# select-sort phase: the 16 key-image staging loads per thread issued in two batches of 8 instead of one load-wait-write at a time
# baseline (speedup 1.0000x reference)
.LBB0_1360:
	s_barrier
	s_and_saveexec_b64 s[0:1], s[6:7]
	s_cbranch_execz .LBB0_1363
	s_lshl_b32 s20, s35, 8
	s_movk_i32 s21, 0x210
	v_ashrrev_i32_e32 v250, 5, v52
	v_and_b32_e32 v192, 0x1f0, v154
	v_mul_lo_u32 v253, v250, s21
	v_add3_u32 v253, 0, v253, v192
	v_add_u32_e32 v250, s20, v250
	v_ashrrev_i32_e32 v251, 31, v250
	v_lshlrev_b64 v[250:251], 9, v[250:251]
	v_lshl_add_u64 v[250:251], s[2:3], 0, v[250:251]
	v_lshl_add_u64 v[250:251], v[250:251], 0, v[192:193]
	s_mov_b64 s[100:101], 0x2000
	global_load_dwordx4 v[218:221], v[250:251], off
	v_lshl_add_u64 v[250:251], v[250:251], 0, s[100:101]
	global_load_dwordx4 v[222:225], v[250:251], off
	v_lshl_add_u64 v[250:251], v[250:251], 0, s[100:101]
	global_load_dwordx4 v[226:229], v[250:251], off
	v_lshl_add_u64 v[250:251], v[250:251], 0, s[100:101]
	global_load_dwordx4 v[230:233], v[250:251], off
	v_lshl_add_u64 v[250:251], v[250:251], 0, s[100:101]
	global_load_dwordx4 v[234:237], v[250:251], off
	v_lshl_add_u64 v[250:251], v[250:251], 0, s[100:101]
	global_load_dwordx4 v[238:241], v[250:251], off
	v_lshl_add_u64 v[250:251], v[250:251], 0, s[100:101]
	global_load_dwordx4 v[242:245], v[250:251], off
	v_lshl_add_u64 v[250:251], v[250:251], 0, s[100:101]
	global_load_dwordx4 v[246:249], v[250:251], off
	v_lshl_add_u64 v[250:251], v[250:251], 0, s[100:101]
	s_waitcnt vmcnt(7)
	ds_write_b128 v253, v[218:221]
	s_waitcnt vmcnt(6)
	ds_write_b128 v253, v[222:225] offset:8448
	s_waitcnt vmcnt(5)
	ds_write_b128 v253, v[226:229] offset:16896
	s_waitcnt vmcnt(4)
	ds_write_b128 v253, v[230:233] offset:25344
	s_waitcnt vmcnt(3)
	ds_write_b128 v253, v[234:237] offset:33792
	s_waitcnt vmcnt(2)
	ds_write_b128 v253, v[238:241] offset:42240
	s_waitcnt vmcnt(1)
	ds_write_b128 v253, v[242:245] offset:50688
	s_waitcnt vmcnt(0)
	ds_write_b128 v253, v[246:249] offset:59136
	v_add_u32_e32 v253, 0x10800, v253
	s_waitcnt lgkmcnt(0)
	global_load_dwordx4 v[218:221], v[250:251], off
	v_lshl_add_u64 v[250:251], v[250:251], 0, s[100:101]
	global_load_dwordx4 v[222:225], v[250:251], off
	v_lshl_add_u64 v[250:251], v[250:251], 0, s[100:101]
	global_load_dwordx4 v[226:229], v[250:251], off
	v_lshl_add_u64 v[250:251], v[250:251], 0, s[100:101]
	global_load_dwordx4 v[230:233], v[250:251], off
	v_lshl_add_u64 v[250:251], v[250:251], 0, s[100:101]
	global_load_dwordx4 v[234:237], v[250:251], off
	v_lshl_add_u64 v[250:251], v[250:251], 0, s[100:101]
	global_load_dwordx4 v[238:241], v[250:251], off
	v_lshl_add_u64 v[250:251], v[250:251], 0, s[100:101]
	global_load_dwordx4 v[242:245], v[250:251], off
	v_lshl_add_u64 v[250:251], v[250:251], 0, s[100:101]
	global_load_dwordx4 v[246:249], v[250:251], off
	v_lshl_add_u64 v[250:251], v[250:251], 0, s[100:101]
	s_waitcnt vmcnt(7)
	ds_write_b128 v253, v[218:221]
	s_waitcnt vmcnt(6)
	ds_write_b128 v253, v[222:225] offset:8448
	s_waitcnt vmcnt(5)
	ds_write_b128 v253, v[226:229] offset:16896
	s_waitcnt vmcnt(4)
	ds_write_b128 v253, v[230:233] offset:25344
	s_waitcnt vmcnt(3)
	ds_write_b128 v253, v[234:237] offset:33792
	s_waitcnt vmcnt(2)
	ds_write_b128 v253, v[238:241] offset:42240
	s_waitcnt vmcnt(1)
	ds_write_b128 v253, v[242:245] offset:50688
	s_waitcnt vmcnt(0)
	ds_write_b128 v253, v[246:249] offset:59136
